# speedup vs baseline: 1.0123x; 1.0084x over previous
_Z11prep_kernelPKfPjPfS1_:
	s_load_dwordx4 s[4:7], s[0:1], 0x0
	v_or_b32_e32 v1, s2, v0
	v_cmp_eq_u32_e32 vcc, 0, v1
	s_and_saveexec_b64 s[8:9], vcc
	s_cbranch_execz .LBB0_2
	s_load_dwordx2 s[10:11], s[0:1], 0x18
	v_mov_b32_e32 v1, 0
	s_waitcnt lgkmcnt(0)
	global_store_dword v1, v1, s[10:11]
	global_store_dword v1, v1, s[10:11] offset:-4096
	global_store_dword v1, v1, s[10:11] offset:-4092
	global_store_dword v1, v1, s[10:11] offset:-4088
	global_store_dword v1, v1, s[10:11] offset:-4084
	global_store_dword v1, v1, s[10:11] offset:-4080
	global_store_dword v1, v1, s[10:11] offset:-4076
	global_store_dword v1, v1, s[10:11] offset:-4072
	global_store_dword v1, v1, s[10:11] offset:-4068
	global_store_dword v1, v1, s[10:11] offset:-4064
	global_store_dword v1, v1, s[10:11] offset:-4060

.LBB1_105:
	s_or_b64 exec, exec, s[2:3]
	s_andn2_b64 vcc, exec, s[36:37]
	s_waitcnt lgkmcnt(0)
	s_barrier
	s_cbranch_vccnz .LBB1_118
	v_lshl_or_b32 v8, v196, 7, v197
	ds_read_b32 v8, v8 offset:36864
	s_waitcnt lgkmcnt(0)
	v_cmp_lt_f32_e32 vcc, 0, v8
	v_lshl_or_b32 v9, v196, 7, v197
	ds_read_b32 v9, v9 offset:37376
	s_waitcnt lgkmcnt(0)
	v_log_f32_e32 v9, v9
	s_nop 1
	v_cndmask_b32_e32 v9, 0, v9, vcc
	s_nop 1
	v_add_f32_dpp v9, v9, v9 quad_perm:[1,0,3,2] row_mask:0xf bank_mask:0xf bound_ctrl:1
	s_nop 1
	v_add_f32_dpp v9, v9, v9 quad_perm:[2,3,0,1] row_mask:0xf bank_mask:0xf bound_ctrl:1
	s_nop 1
	v_add_f32_dpp v9, v9, v9 row_half_mirror row_mask:0xf bank_mask:0xf bound_ctrl:1
	s_nop 1
	v_add_f32_dpp v9, v9, v9 row_mirror row_mask:0xf bank_mask:0xf bound_ctrl:1
	s_nop 1
	v_add_f32_dpp v9, v9, v9 row_bcast:15 row_mask:0xa bank_mask:0xf bound_ctrl:1
	s_nop 1
	v_add_f32_dpp v9, v9, v9 row_bcast:31 row_mask:0xc bank_mask:0xf bound_ctrl:1
	s_nop 1
	v_readlane_b32 s16, v9, 63
	s_nop 3
	s_and_saveexec_b64 s[2:3], s[0:1]
	s_cbranch_execz .LBB1_118
	v_mov_b32_e32 v8, 0
	ds_read_b128 v[10:13], v8 offset:37632
	ds_read_b128 v[14:17], v8 offset:37648
	s_bcnt1_i32_b64 s4, vcc
	v_readlane_b32 s6, v240, 0
	v_readlane_b32 s10, v240, 12
	v_readlane_b32 s11, v240, 13
	v_readlane_b32 s12, v240, 4
	v_readlane_b32 s13, v240, 5
	s_lshr_b32 s6, s6, 7
	s_lshl_b32 s6, s6, 3
	s_add_u32 s8, s10, s6
	s_addc_u32 s9, s11, 0
	s_waitcnt lgkmcnt(0)
	v_add_f32_e32 v9, 0, v10
	v_add_f32_e32 v9, v9, v11
	v_add_f32_e32 v9, v9, v12
	v_add_f32_e32 v9, v9, v13
	v_add_f32_e32 v9, v9, v14
	v_add_f32_e32 v9, v9, v15
	v_add_f32_e32 v9, v9, v16
	v_add_f32_e32 v9, v9, v17
	v_subrev_f32_e32 v9, s16, v9
	v_mul_f32_e32 v9, 0x3f317218, v9
	v_max_f32_e32 v9, 0, v9
	v_floor_f32_e32 v10, v9
	v_sub_f32_e32 v11, v9, v10
	v_cvt_u32_f32_e32 v10, v10
	v_mul_f32_e32 v11, 0x4a800000, v11
	v_cvt_u32_f32_e32 v11, v11
	v_lshrrev_b32_e32 v12, 8, v11
	v_lshl_or_b32 v13, v10, 14, v12
	v_lshlrev_b32_e32 v12, 24, v11
	s_lshl_b32 s5, s4, 8
	s_or_b32 s5, s5, 1
	v_or_b32_e32 v12, s5, v12
	global_atomic_add_x2 v[14:15], v8, v[12:13], s[8:9] sc0
	s_waitcnt vmcnt(0)
	v_and_b32_e32 v16, 0xff, v14
	s_nop 0
	v_readfirstlane_b32 s5, v16
	s_cmp_lg_u32 s5, 63
	s_cbranch_scc1 .LBB1_118
	v_add_co_u32_e32 v14, vcc, v14, v12
	s_nop 1
	v_addc_co_u32_e32 v15, vcc, v15, v13, vcc
	v_cvt_f32_u32_e32 v2, v15
	v_lshrrev_b32_e32 v3, 24, v14
	v_cvt_f32_u32_e32 v3, v3
	v_mul_f32_e32 v2, 0x38800000, v2
	v_mul_f32_e32 v3, 0x34800000, v3
	v_add_f32_e32 v2, v2, v3
	v_bfe_u32 v3, v14, 8, 16
	v_cvt_f32_u32_e32 v3, v3
	v_max_f32_e32 v3, 0x358637bd, v3
	v_div_scale_f32 v4, s[14:15], v3, v3, v2
	v_rcp_f32_e32 v5, v4
	s_nop 0
	v_fma_f32 v6, -v4, v5, 1.0
	v_fmac_f32_e32 v5, v6, v5
	v_div_scale_f32 v6, vcc, v2, v3, v2
	v_mul_f32_e32 v7, v6, v5
	v_fma_f32 v9, -v4, v7, v6
	v_fmac_f32_e32 v7, v9, v5
	v_fma_f32 v4, -v4, v7, v6
	v_div_fmas_f32 v4, v4, v5, v7
	v_div_fixup_f32 v2, v4, v3, v2
	v_floor_f32_e32 v4, v2
	v_sub_f32_e32 v5, v2, v4
	v_cvt_u32_f32_e32 v4, v4
	v_mul_f32_e32 v5, 0x4e800000, v5
	v_cvt_u32_f32_e32 v5, v5
	v_lshl_or_b32 v6, v4, 30, v5
	v_lshrrev_b32_e32 v7, 2, v4
	v_lshrrev_b32_e32 v5, 24, v6
	v_lshl_or_b32 v7, v7, 8, v5
	v_lshlrev_b32_e32 v6, 8, v6
	v_or_b32_e32 v6, 1, v6
	global_atomic_add_x2 v[10:11], v8, v[6:7], s[10:11] offset:32 sc0
	s_waitcnt vmcnt(0)
	v_and_b32_e32 v12, 0xff, v10
	s_nop 0
	v_readfirstlane_b32 s5, v12
	s_cmp_lg_u32 s5, 3
	s_cbranch_scc1 .LBB1_118
	v_add_co_u32_e32 v10, vcc, v10, v6
	s_nop 1
	v_addc_co_u32_e32 v11, vcc, v11, v7, vcc
	v_cvt_f32_u32_e32 v2, v11
	v_lshrrev_b32_e32 v3, 8, v10
	v_cvt_f32_u32_e32 v3, v3
	v_mul_f32_e32 v2, 0x4b800000, v2
	v_add_f32_e32 v2, v2, v3
	v_mul_f32_e32 v2, 0x2f800000, v2
	global_store_dword v8, v2, s[12:13]
